# v75 + P10 emission loop restructured: rows handled two at a time with full EXEC, one rare-path test per row pair, candidate blocks out of line
# baseline (speedup 1.0000x reference)
.LBB0_1228:
	global_load_dwordx2 v[10:11], v[12:13], off sc1
	global_load_dwordx2 v[8:9], v[12:13], off offset:256 sc1
	s_waitcnt vmcnt(3)
	v_cmp_le_f16_e64 s[50:51], s43, v16
	v_cmp_le_f16_e64 s[52:53], s86, v16
	v_cmp_le_f16_sdwa s[54:55], s47, v16 src0_sel:DWORD src1_sel:WORD_1
	v_cmp_le_f16_sdwa s[56:57], s46, v16 src0_sel:DWORD src1_sel:WORD_1
	v_mbcnt_lo_u32_b32 v20, s50, 0
	v_mbcnt_lo_u32_b32 v21, s54, 0
	v_mbcnt_hi_u32_b32 v20, s51, v20
	v_mbcnt_hi_u32_b32 v21, s55, v21
	v_add_u32_e32 v20, s76, v20
	v_add_u32_e32 v21, s73, v21
	v_cmp_gt_i32_e64 s[58:59], s48, v20
	v_cmp_gt_i32_e64 s[60:61], s48, v21
	v_lshl_add_u32 v20, v20, 1, s33
	v_lshl_add_u32 v21, v21, 1, s88
	s_and_b64 exec, s[50:51], s[58:59]
	ds_write_b16 v20, v18 offset:24576
	s_and_b64 exec, s[54:55], s[60:61]
	ds_write_b16 v21, v18 offset:24576
	s_mov_b64 exec, -1
	s_bcnt1_i32_b64 s0, s[50:51]
	s_add_i32 s76, s76, s0
	s_bcnt1_i32_b64 s0, s[54:55]
	s_add_i32 s73, s73, s0
	s_andn2_b64 s[52:53], s[52:53], s[50:51]
	s_andn2_b64 s[56:57], s[56:57], s[54:55]
	s_or_b64 s[0:1], s[52:53], s[56:57]
	s_cmp_eq_u64 s[0:1], 0
	s_cbranch_scc0 .Lem_slow_0
.Lem_back_0:
	v_cmp_le_f16_e64 s[50:51], s39, v17
	v_cmp_le_f16_e64 s[52:53], s38, v17
	v_cmp_le_f16_sdwa s[54:55], s37, v17 src0_sel:DWORD src1_sel:WORD_1
	v_cmp_le_f16_sdwa s[56:57], s36, v17 src0_sel:DWORD src1_sel:WORD_1
	v_mbcnt_lo_u32_b32 v20, s50, 0
	v_mbcnt_lo_u32_b32 v21, s54, 0
	v_mbcnt_hi_u32_b32 v20, s51, v20
	v_mbcnt_hi_u32_b32 v21, s55, v21
	v_add_u32_e32 v20, s84, v20
	v_add_u32_e32 v21, s85, v21
	v_cmp_gt_i32_e64 s[58:59], s48, v20
	v_cmp_gt_i32_e64 s[60:61], s48, v21
	v_lshl_add_u32 v20, v20, 1, s91
	v_lshl_add_u32 v21, v21, 1, s15
	s_and_b64 exec, s[50:51], s[58:59]
	ds_write_b16 v20, v18 offset:24576
	s_and_b64 exec, s[54:55], s[60:61]
	ds_write_b16 v21, v18 offset:24576
	s_mov_b64 exec, -1
	s_bcnt1_i32_b64 s0, s[50:51]
	s_add_i32 s84, s84, s0
	s_bcnt1_i32_b64 s0, s[54:55]
	s_add_i32 s85, s85, s0
	s_andn2_b64 s[52:53], s[52:53], s[50:51]
	s_andn2_b64 s[56:57], s[56:57], s[54:55]
	s_or_b64 s[0:1], s[52:53], s[56:57]
	s_cmp_eq_u64 s[0:1], 0
	s_cbranch_scc0 .Lem_slow_1
.Lem_back_1:
	s_waitcnt vmcnt(2)
	v_cmp_le_f16_e64 s[50:51], s35, v14
	v_cmp_le_f16_e64 s[52:53], s34, v14
	v_cmp_le_f16_sdwa s[54:55], s31, v14 src0_sel:DWORD src1_sel:WORD_1
	v_cmp_le_f16_sdwa s[56:57], s30, v14 src0_sel:DWORD src1_sel:WORD_1
	v_mbcnt_lo_u32_b32 v20, s50, 0
	v_mbcnt_lo_u32_b32 v21, s54, 0
	v_mbcnt_hi_u32_b32 v20, s51, v20
	v_mbcnt_hi_u32_b32 v21, s55, v21
	v_add_u32_e32 v20, s24, v20
	v_add_u32_e32 v21, s25, v21
	v_cmp_gt_i32_e64 s[58:59], s48, v20
	v_cmp_gt_i32_e64 s[60:61], s48, v21
	v_lshl_add_u32 v20, v20, 1, s17
	v_lshl_add_u32 v21, v21, 1, s19
	s_and_b64 exec, s[50:51], s[58:59]
	ds_write_b16 v20, v18 offset:24576
	s_and_b64 exec, s[54:55], s[60:61]
	ds_write_b16 v21, v18 offset:24576
	s_mov_b64 exec, -1
	s_bcnt1_i32_b64 s0, s[50:51]
	s_add_i32 s24, s24, s0
	s_bcnt1_i32_b64 s0, s[54:55]
	s_add_i32 s25, s25, s0
	s_andn2_b64 s[52:53], s[52:53], s[50:51]
	s_andn2_b64 s[56:57], s[56:57], s[54:55]
	s_or_b64 s[0:1], s[52:53], s[56:57]
	s_cmp_eq_u64 s[0:1], 0
	s_cbranch_scc0 .Lem_slow_2
.Lem_back_2:
	v_cmp_le_f16_e64 s[50:51], s79, v15
	v_cmp_le_f16_e64 s[52:53], s78, v15
	v_cmp_le_f16_sdwa s[54:55], s29, v15 src0_sel:DWORD src1_sel:WORD_1
	v_cmp_le_f16_sdwa s[56:57], s28, v15 src0_sel:DWORD src1_sel:WORD_1
	v_mbcnt_lo_u32_b32 v20, s50, 0
	v_mbcnt_lo_u32_b32 v21, s54, 0
	v_mbcnt_hi_u32_b32 v20, s51, v20
	v_mbcnt_hi_u32_b32 v21, s55, v21
	v_add_u32_e32 v20, s26, v20
	v_add_u32_e32 v21, s27, v21
	v_cmp_gt_i32_e64 s[58:59], s48, v20
	v_cmp_gt_i32_e64 s[60:61], s48, v21
	v_lshl_add_u32 v20, v20, 1, s21
	v_lshl_add_u32 v21, v21, 1, s23
	s_and_b64 exec, s[50:51], s[58:59]
	ds_write_b16 v20, v18 offset:24576
	s_and_b64 exec, s[54:55], s[60:61]
	ds_write_b16 v21, v18 offset:24576
	s_mov_b64 exec, -1
	s_bcnt1_i32_b64 s0, s[50:51]
	s_add_i32 s26, s26, s0
	s_bcnt1_i32_b64 s0, s[54:55]
	s_add_i32 s27, s27, s0
	s_andn2_b64 s[52:53], s[52:53], s[50:51]
	s_andn2_b64 s[56:57], s[56:57], s[54:55]
	s_or_b64 s[0:1], s[52:53], s[56:57]
	s_cmp_eq_u64 s[0:1], 0
	s_cbranch_scc0 .Lem_slow_3
.Lem_back_3:
	s_add_i32 s75, s75, -1
	v_subrev_u32_e32 v19, 64, v19
	v_add_u32_e32 v18, 64, v18
	s_cmp_eq_u32 s75, 0
	v_lshl_add_u64 v[12:13], v[12:13], 0, s[92:93]
	s_cbranch_scc1 .LBB0_1301
	s_waitcnt vmcnt(1)
	v_mov_b64_e32 v[16:17], v[10:11]
	s_waitcnt vmcnt(0)
	v_mov_b64_e32 v[14:15], v[8:9]
	s_branch .LBB0_1228
.Lem_slow_0:
	v_cmp_le_f16_e32 vcc, s43, v16
	v_cmp_le_f16_e64 s[50:51], s86, v16
	s_andn2_b64 s[52:53], s[50:51], vcc
	s_cmp_eq_u64 s[52:53], 0
	s_cbranch_scc1 .Lem_skip_0
	s_xor_b64 s[0:1], s[50:51], -1
	s_nor_b64 s[0:1], vcc, s[0:1]
	s_and_saveexec_b64 s[54:55], s[0:1]
	s_cbranch_execz .LBB0_1235
	v_mbcnt_lo_u32_b32 v20, s52, v0
	v_mbcnt_hi_u32_b32 v20, s53, v20
	v_cmp_gt_i32_e64 s[50:51], s49, v20
	s_and_b64 exec, exec, s[50:51]
	s_cbranch_execz .LBB0_1235
	v_and_b32_e32 v21, 0xffff, v16
	v_cmp_ne_u32_e64 s[50:51], s42, v21
	v_lshl_add_u32 v20, v20, 2, s89
	s_nop 0
	v_cndmask_b32_e64 v21, 0, v21, s[50:51]
	v_cmp_gt_u32_e64 s[50:51], s42, v21
	s_nop 1
	v_cndmask_b32_e64 v22, v186, v187, s[50:51]
	v_xor_b32_e32 v21, v22, v21
	v_lshl_or_b32 v21, v21, 16, v19
	ds_write_b32 v20, v21

.Lem_skip_0:
	v_cmp_le_f16_sdwa s[64:65], s47, v16 src0_sel:DWORD src1_sel:WORD_1
	v_cmp_le_f16_sdwa s[54:55], s46, v16 src0_sel:DWORD src1_sel:WORD_1
	s_andn2_b64 s[52:53], s[54:55], s[64:65]
	s_cmp_eq_u64 s[52:53], 0
	s_cbranch_scc1 .Lem_skip_1
	s_xor_b64 s[0:1], s[54:55], -1
	s_nor_b64 s[0:1], s[64:65], s[0:1]
	s_and_saveexec_b64 s[50:51], s[0:1]
	s_xor_b64 s[54:55], exec, s[50:51]
	s_cbranch_execz .LBB0_1244
	v_mbcnt_lo_u32_b32 v20, s52, v1
	v_mbcnt_hi_u32_b32 v20, s53, v20
	v_cmp_gt_i32_e64 s[50:51], s49, v20
	s_and_saveexec_b64 s[0:1], s[50:51]
	s_cbranch_execz .LBB0_1243
	v_lshrrev_b64 v[22:23], 16, v[16:17]
	v_and_b32_e32 v16, 0xffff, v22
	v_cmp_ne_u32_e64 s[50:51], s42, v16
	v_lshl_add_u32 v20, v20, 2, s40
	s_nop 0
	v_cndmask_b32_e64 v16, 0, v16, s[50:51]
	v_cmp_gt_u32_e64 s[50:51], s42, v16
	s_nop 1
	v_cndmask_b32_e64 v21, v186, v187, s[50:51]
	v_xor_b32_e32 v16, v21, v16
	v_lshl_or_b32 v16, v16, 16, v19
	ds_write_b32 v20, v16

.LBB0_1244:
	s_andn2_saveexec_b64 s[0:1], s[54:55]
	s_or_b64 exec, exec, s[0:1]
	s_bcnt1_i32_b64 s0, s[52:53]
	v_add_u32_e32 v1, s0, v1
.Lem_skip_1:
	s_branch .Lem_back_0
.Lem_slow_1:
	v_cmp_le_f16_e64 s[50:51], s39, v17
	v_cmp_le_f16_e64 s[52:53], s38, v17
	s_andn2_b64 s[54:55], s[52:53], s[50:51]
	s_cmp_eq_u64 s[54:55], 0
	s_cbranch_scc1 .Lem_skip_2
	s_xor_b64 s[0:1], s[52:53], -1
	s_nor_b64 s[0:1], s[50:51], s[0:1]
	s_and_saveexec_b64 s[52:53], s[0:1]
	s_xor_b64 s[56:57], exec, s[52:53]
	s_cbranch_execz .LBB0_1253
	v_mbcnt_lo_u32_b32 v16, s54, v2
	v_mbcnt_hi_u32_b32 v16, s55, v16
	v_cmp_gt_i32_e64 s[52:53], s49, v16
	s_and_saveexec_b64 s[0:1], s[52:53]
	s_cbranch_execz .LBB0_1252
	v_and_b32_e32 v20, 0xffff, v17
	v_cmp_ne_u32_e64 s[52:53], s42, v20
	s_nop 1
	v_cndmask_b32_e64 v20, 0, v20, s[52:53]
	v_cmp_gt_u32_e64 s[52:53], s42, v20
	s_nop 1
	v_cndmask_b32_e64 v21, v186, v187, s[52:53]
	v_xor_b32_e32 v20, v21, v20
	v_readlane_b32 s52, v254, 34
	v_lshl_or_b32 v20, v20, 16, v19
	s_nop 0
	v_lshl_add_u32 v16, v16, 2, s52
	ds_write_b32 v16, v20

.Lem_skip_2:
	v_lshrrev_b32_e32 v52, 16, v17
	v_cmp_le_f16_e64 s[52:53], s37, v52
	v_cmp_le_f16_e64 s[54:55], s36, v52
	s_andn2_b64 s[56:57], s[54:55], s[52:53]
	s_cmp_eq_u64 s[56:57], 0
	s_cbranch_scc1 .Lem_skip_3
	s_xor_b64 s[0:1], s[54:55], -1
	s_nor_b64 s[0:1], s[52:53], s[0:1]
	s_and_saveexec_b64 s[54:55], s[0:1]
	s_xor_b64 s[58:59], exec, s[54:55]
	s_cbranch_execz .LBB0_1262
	v_mbcnt_lo_u32_b32 v16, s56, v3
	v_mbcnt_hi_u32_b32 v16, s57, v16
	v_cmp_gt_i32_e64 s[54:55], s49, v16
	s_and_saveexec_b64 s[0:1], s[54:55]
	s_cbranch_execz .LBB0_1261
	v_cmp_ne_u64_e64 s[54:55], s[94:95], v[52:53]
	s_nop 1
	v_cndmask_b32_e64 v17, 0, v52, s[54:55]
	v_cmp_gt_u32_e64 s[54:55], s42, v17
	s_nop 1
	v_cndmask_b32_e64 v20, v186, v187, s[54:55]
	v_xor_b32_e32 v17, v20, v17
	v_readlane_b32 s54, v254, 35
	v_lshl_or_b32 v17, v17, 16, v19
	s_nop 0
	v_lshl_add_u32 v16, v16, 2, s54
	ds_write_b32 v16, v17

.LBB0_1262:
	s_andn2_saveexec_b64 s[0:1], s[58:59]
	s_or_b64 exec, exec, s[0:1]
	s_bcnt1_i32_b64 s0, s[56:57]
	v_add_u32_e32 v3, s0, v3
.Lem_skip_3:
	s_branch .Lem_back_1
.Lem_slow_2:
	v_cmp_le_f16_e64 s[54:55], s35, v14
	v_cmp_le_f16_e64 s[56:57], s34, v14
	s_andn2_b64 s[58:59], s[56:57], s[54:55]
	s_cmp_eq_u64 s[58:59], 0
	s_cbranch_scc1 .Lem_skip_4
	s_xor_b64 s[0:1], s[56:57], -1
	s_nor_b64 s[0:1], s[54:55], s[0:1]
	s_and_saveexec_b64 s[56:57], s[0:1]
	s_xor_b64 s[60:61], exec, s[56:57]
	s_cbranch_execz .LBB0_1271
	v_mbcnt_lo_u32_b32 v16, s58, v4
	v_mbcnt_hi_u32_b32 v16, s59, v16
	v_cmp_gt_i32_e64 s[56:57], s49, v16
	s_and_saveexec_b64 s[0:1], s[56:57]
	s_cbranch_execz .LBB0_1270
	v_and_b32_e32 v17, 0xffff, v14
	v_cmp_ne_u32_e64 s[56:57], s42, v17
	v_lshl_add_u32 v16, v16, 2, s18
	s_nop 0
	v_cndmask_b32_e64 v17, 0, v17, s[56:57]
	v_cmp_gt_u32_e64 s[56:57], s42, v17
	s_nop 1
	v_cndmask_b32_e64 v20, v186, v187, s[56:57]
	v_xor_b32_e32 v17, v20, v17
	v_lshl_or_b32 v17, v17, 16, v19
	ds_write_b32 v16, v17

.Lem_skip_4:
	v_cmp_le_f16_sdwa s[66:67], s31, v14 src0_sel:DWORD src1_sel:WORD_1
	v_cmp_le_f16_sdwa s[60:61], s30, v14 src0_sel:DWORD src1_sel:WORD_1
	s_andn2_b64 s[58:59], s[60:61], s[66:67]
	s_cmp_eq_u64 s[58:59], 0
	s_cbranch_scc1 .Lem_skip_5
	s_xor_b64 s[0:1], s[60:61], -1
	s_nor_b64 s[0:1], s[66:67], s[0:1]
	s_and_saveexec_b64 s[56:57], s[0:1]
	s_xor_b64 s[60:61], exec, s[56:57]
	s_cbranch_execz .LBB0_1280
	v_mbcnt_lo_u32_b32 v16, s58, v5
	v_mbcnt_hi_u32_b32 v16, s59, v16
	v_cmp_gt_i32_e64 s[56:57], s49, v16
	s_and_saveexec_b64 s[0:1], s[56:57]
	s_cbranch_execz .LBB0_1279
	v_lshrrev_b64 v[20:21], 16, v[14:15]
	v_and_b32_e32 v14, 0xffff, v20
	v_cmp_ne_u32_e64 s[56:57], s42, v14
	v_lshl_add_u32 v16, v16, 2, s20
	s_nop 0
	v_cndmask_b32_e64 v14, 0, v14, s[56:57]
	v_cmp_gt_u32_e64 s[56:57], s42, v14
	s_nop 1
	v_cndmask_b32_e64 v17, v186, v187, s[56:57]
	v_xor_b32_e32 v14, v17, v14
	v_lshl_or_b32 v14, v14, 16, v19
	ds_write_b32 v16, v14

.LBB0_1280:
	s_andn2_saveexec_b64 s[0:1], s[60:61]
	s_or_b64 exec, exec, s[0:1]
	s_bcnt1_i32_b64 s0, s[58:59]
	v_add_u32_e32 v5, s0, v5
.Lem_skip_5:
	s_branch .Lem_back_2
.Lem_slow_3:
	v_cmp_le_f16_e64 s[56:57], s79, v15
	v_cmp_le_f16_e64 s[58:59], s78, v15
	s_andn2_b64 s[60:61], s[58:59], s[56:57]
	s_cmp_eq_u64 s[60:61], 0
	s_cbranch_scc1 .Lem_skip_6
	s_xor_b64 s[0:1], s[58:59], -1
	s_nor_b64 s[0:1], s[56:57], s[0:1]
	s_and_saveexec_b64 s[58:59], s[0:1]
	s_xor_b64 s[62:63], exec, s[58:59]
	s_cbranch_execz .LBB0_1289
	v_mbcnt_lo_u32_b32 v14, s60, v6
	v_mbcnt_hi_u32_b32 v14, s61, v14
	v_cmp_gt_i32_e64 s[58:59], s49, v14
	s_and_saveexec_b64 s[0:1], s[58:59]
	s_cbranch_execz .LBB0_1288
	v_and_b32_e32 v16, 0xffff, v15
	v_cmp_ne_u32_e64 s[58:59], s42, v16
	v_lshl_add_u32 v14, v14, 2, s90
	s_nop 0
	v_cndmask_b32_e64 v16, 0, v16, s[58:59]
	v_cmp_gt_u32_e64 s[58:59], s42, v16
	s_nop 1
	v_cndmask_b32_e64 v17, v186, v187, s[58:59]
	v_xor_b32_e32 v16, v17, v16
	v_lshl_or_b32 v16, v16, 16, v19
	ds_write_b32 v14, v16

.Lem_skip_6:
	v_lshrrev_b32_e32 v52, 16, v15
	v_cmp_le_f16_e64 s[58:59], s29, v52
	v_cmp_le_f16_e64 s[60:61], s28, v52
	s_andn2_b64 s[62:63], s[60:61], s[58:59]
	s_cmp_eq_u64 s[62:63], 0
	s_cbranch_scc1 .Lem_skip_7
	s_xor_b64 s[0:1], s[60:61], -1
	s_nor_b64 s[0:1], s[58:59], s[0:1]
	s_and_saveexec_b64 s[60:61], s[0:1]
	s_xor_b64 s[68:69], exec, s[60:61]
	s_cbranch_execz .LBB0_1298
	v_mbcnt_lo_u32_b32 v14, s62, v7
	v_mbcnt_hi_u32_b32 v14, s63, v14
	v_cmp_gt_i32_e64 s[60:61], s49, v14
	s_and_saveexec_b64 s[0:1], s[60:61]
	s_cbranch_execz .LBB0_1297
	v_cmp_ne_u64_e64 s[60:61], s[94:95], v[52:53]
	v_lshl_add_u32 v14, v14, 2, s22
	s_nop 0
	v_cndmask_b32_e64 v15, 0, v52, s[60:61]
	v_cmp_gt_u32_e64 s[60:61], s42, v15
	s_nop 1
	v_cndmask_b32_e64 v16, v186, v187, s[60:61]
	v_xor_b32_e32 v15, v16, v15
	v_lshl_or_b32 v15, v15, 16, v19
	ds_write_b32 v14, v15

.LBB0_1298:
	s_andn2_saveexec_b64 s[0:1], s[68:69]
	s_or_b64 exec, exec, s[0:1]
	s_bcnt1_i32_b64 s0, s[62:63]
	v_add_u32_e32 v7, s0, v7
.Lem_skip_7:
	s_branch .Lem_back_3
.LBB0_1301:
	v_readlane_b32 s54, v255, 4
	s_waitcnt vmcnt(1)
	v_cmp_le_f16_e64 s[50:51], s43, v10
	v_readlane_b32 s55, v255, 5
	v_cmp_le_f16_e64 s[52:53], s86, v10
	s_and_b64 s[0:1], s[54:55], s[50:51]
	v_cndmask_b32_e64 v12, 0, 1, s[0:1]
	s_and_b64 s[56:57], s[54:55], s[52:53]
	v_cmp_ne_u32_e32 vcc, 0, v12
	v_cndmask_b32_e64 v12, 0, 1, s[56:57]
	v_add_u32_e32 v13, s87, v138
	v_cmp_ne_u32_e64 s[52:53], 0, v12
	s_and_saveexec_b64 s[58:59], s[0:1]
	s_cbranch_execz .LBB0_1304
	v_mov_b32_e32 v12, s76
	v_mbcnt_lo_u32_b32 v12, vcc_lo, v12
	v_mbcnt_hi_u32_b32 v12, vcc_hi, v12
	v_cmp_gt_i32_e64 s[54:55], s48, v12
	s_and_b64 exec, exec, s[54:55]
	v_lshl_add_u32 v12, v12, 1, s33
	ds_write_b16 v12, v13 offset:24576
